# grid barrier: non-leader workgroups issue their acquire invalidate on arrival (before polling) instead of after the release; they issue no cached load in between
# speedup vs baseline: 1.0056x; 1.0056x over previous
; __device__ __forceinline__ unsigned xb_ld(unsigned* p)              { return __hip_atomic_load(p, __ATOMIC_RELAXED, __HIP_MEMORY_SCOPE_AGENT); }
; __device__ __forceinline__ unsigned xb_add(unsigned* p, unsigned v) { return __hip_atomic_fetch_add(p, v, __ATOMIC_RELAXED, __HIP_MEMORY_SCOPE_AGENT); }
; #define XB_SPIN(cond, bar) do { unsigned _sp = 0; while (cond) { __builtin_amdgcn_s_sleep(1); \
;     if ((++_sp & 255u) == 0u) { if (xb_ld(&(bar)[XB_TMO])) break; if (_sp > XB_SPIN_CAP) { atomicAdd(&(bar)[XB_TMO], 1u); break; } } } } while (0)
; __device__ __forceinline__ void xcd_barrier(const XcdBarrier& b) {
;     ...
;         const unsigned old = xb_add(&bar[XB_XSUB(b.x)], 1u);
;         const unsigned gen = old / nloc;
;         if (old + 1u == (gen + 1u) * nloc) {
;             __builtin_amdgcn_fence(__ATOMIC_RELEASE, "agent");
;             asm volatile("s_waitcnt vmcnt(0)" ::: "memory");
;             const unsigned og = xb_add(&bar[XB_TOP], 1u);
;             const unsigned tg = og / nx;
;             if (og + 1u == (tg + 1u) * nx) xb_add(&bar[XB_TOPGEN], 1u);
;             else XB_SPIN(xb_ld(&bar[XB_TOPGEN]) == tg, bar);
;             __builtin_amdgcn_fence(__ATOMIC_ACQUIRE, "agent");
;             xb_add(&bar[XB_XGEN(b.x)], 1u);
;             asm volatile("s_waitcnt vmcnt(0)" ::: "memory");
;         } else {
;             XB_SPIN(xb_ld(&bar[XB_XGEN(b.x)]) == gen, bar);
;             __builtin_amdgcn_fence(__ATOMIC_ACQUIRE, "agent");
;             asm volatile("s_waitcnt vmcnt(0)" ::: "memory");
;         }
.LBB0_439:
	s_or_b64 exec, exec, s[8:9]
	v_cvt_f32_u32_e32 v6, v4
	s_waitcnt vmcnt(0)
	v_readfirstlane_b32 s6, v5
	v_sub_u32_e32 v5, 0, v4
	v_rcp_iflag_f32_e32 v6, v6
	v_add_u32_e32 v7, s6, v3
	v_mul_f32_e32 v6, 0x4f7ffffe, v6
	v_cvt_u32_f32_e32 v6, v6
	v_mul_lo_u32 v3, v5, v6
	v_mul_hi_u32 v3, v6, v3
	v_add_u32_e32 v3, v6, v3
	v_mul_hi_u32 v3, v7, v3
	v_mul_lo_u32 v5, v3, v4
	v_sub_u32_e32 v5, v7, v5
	v_add_u32_e32 v6, 1, v3
	v_cmp_ge_u32_e32 vcc, v5, v4
	s_nop 1
	v_cndmask_b32_e32 v3, v3, v6, vcc
	v_sub_u32_e32 v6, v5, v4
	v_cndmask_b32_e32 v5, v5, v6, vcc
	v_add_u32_e32 v6, 1, v3
	v_cmp_ge_u32_e32 vcc, v5, v4
	v_add_u32_e32 v5, 1, v7
	s_nop 0
	v_cndmask_b32_e32 v3, v3, v6, vcc
	v_mul_lo_u32 v6, v4, v3
	v_add_u32_e32 v4, v6, v4
	v_cmp_ne_u32_e32 vcc, v5, v4
	s_and_saveexec_b64 s[6:7], vcc
	s_xor_b64 s[6:7], exec, s[6:7]
	s_cbranch_execz .LBB0_453
	s_waitcnt lgkmcnt(0)
	v_mov_b32_e32 v2, 0x2000
	buffer_inv sc1
	global_load_dword v2, v2, s[4:5] offset:1024 sc1
	s_add_u32 s14, s4, 0x2400
	s_addc_u32 s15, s5, 0
	s_waitcnt vmcnt(0)
	v_cmp_eq_u32_e32 vcc, v2, v3
	s_and_saveexec_b64 s[8:9], vcc
	s_cbranch_execz .LBB0_452
	s_add_u32 s10, s2, 0x4200
	s_addc_u32 s11, s3, 0
	s_mov_b32 s12, 1
	s_mov_b64 s[16:17], 0
	v_mov_b32_e32 v2, 0
	s_branch .LBB0_443

; __device__ __forceinline__ unsigned xb_ld(unsigned* p)              { return __hip_atomic_load(p, __ATOMIC_RELAXED, __HIP_MEMORY_SCOPE_AGENT); }
; #define XB_SPIN(cond, bar) do { unsigned _sp = 0; while (cond) { __builtin_amdgcn_s_sleep(1); \
;     if ((++_sp & 255u) == 0u) { if (xb_ld(&(bar)[XB_TMO])) break; if (_sp > XB_SPIN_CAP) { atomicAdd(&(bar)[XB_TMO], 1u); break; } } } } while (0)
; __device__ __forceinline__ void xcd_barrier(const XcdBarrier& b) {
;     ...
;         } else {
;             XB_SPIN(xb_ld(&bar[XB_XGEN(b.x)]) == gen, bar);
;             __builtin_amdgcn_fence(__ATOMIC_ACQUIRE, "agent");
;             asm volatile("s_waitcnt vmcnt(0)" ::: "memory");
;         }
.LBB0_452:
	s_or_b64 exec, exec, s[8:9]
	s_waitcnt vmcnt(0)
	s_waitcnt vmcnt(0)

; __device__ __forceinline__ unsigned xb_ld(unsigned* p)              { return __hip_atomic_load(p, __ATOMIC_RELAXED, __HIP_MEMORY_SCOPE_AGENT); }
; __device__ __forceinline__ unsigned xb_add(unsigned* p, unsigned v) { return __hip_atomic_fetch_add(p, v, __ATOMIC_RELAXED, __HIP_MEMORY_SCOPE_AGENT); }
; #define XB_SPIN(cond, bar) do { unsigned _sp = 0; while (cond) { __builtin_amdgcn_s_sleep(1); \
;     if ((++_sp & 255u) == 0u) { if (xb_ld(&(bar)[XB_TMO])) break; if (_sp > XB_SPIN_CAP) { atomicAdd(&(bar)[XB_TMO], 1u); break; } } } } while (0)
; __device__ __forceinline__ void xcd_barrier(const XcdBarrier& b) {
;     ...
;         const unsigned old = xb_add(&bar[XB_XSUB(b.x)], 1u);
;         const unsigned gen = old / nloc;
;         if (old + 1u == (gen + 1u) * nloc) {
;             __builtin_amdgcn_fence(__ATOMIC_RELEASE, "agent");
;             asm volatile("s_waitcnt vmcnt(0)" ::: "memory");
;             const unsigned og = xb_add(&bar[XB_TOP], 1u);
;             const unsigned tg = og / nx;
;             if (og + 1u == (tg + 1u) * nx) xb_add(&bar[XB_TOPGEN], 1u);
;             else XB_SPIN(xb_ld(&bar[XB_TOPGEN]) == tg, bar);
;             __builtin_amdgcn_fence(__ATOMIC_ACQUIRE, "agent");
;             xb_add(&bar[XB_XGEN(b.x)], 1u);
;             asm volatile("s_waitcnt vmcnt(0)" ::: "memory");
;         } else {
;             XB_SPIN(xb_ld(&bar[XB_XGEN(b.x)]) == gen, bar);
;             __builtin_amdgcn_fence(__ATOMIC_ACQUIRE, "agent");
;             asm volatile("s_waitcnt vmcnt(0)" ::: "memory");
;         }
.LBB0_521:
	s_or_b64 exec, exec, s[22:23]
	v_cvt_f32_u32_e32 v6, v4
	s_waitcnt vmcnt(0)
	v_readfirstlane_b32 s20, v5
	v_sub_u32_e32 v5, 0, v4
	v_rcp_iflag_f32_e32 v6, v6
	v_add_u32_e32 v7, s20, v1
	v_mul_f32_e32 v6, 0x4f7ffffe, v6
	v_cvt_u32_f32_e32 v6, v6
	v_mul_lo_u32 v1, v5, v6
	v_mul_hi_u32 v1, v6, v1
	v_add_u32_e32 v1, v6, v1
	v_mul_hi_u32 v1, v7, v1
	v_mul_lo_u32 v5, v1, v4
	v_sub_u32_e32 v5, v7, v5
	v_add_u32_e32 v6, 1, v1
	v_cmp_ge_u32_e32 vcc, v5, v4
	s_nop 1
	v_cndmask_b32_e32 v1, v1, v6, vcc
	v_sub_u32_e32 v6, v5, v4
	v_cndmask_b32_e32 v5, v5, v6, vcc
	v_add_u32_e32 v6, 1, v1
	v_cmp_ge_u32_e32 vcc, v5, v4
	v_add_u32_e32 v5, 1, v7
	s_nop 0
	v_cndmask_b32_e32 v1, v1, v6, vcc
	v_mul_lo_u32 v6, v4, v1
	v_add_u32_e32 v4, v6, v4
	v_cmp_ne_u32_e32 vcc, v5, v4
	s_and_saveexec_b64 s[20:21], vcc
	s_xor_b64 s[20:21], exec, s[20:21]
	s_cbranch_execz .LBB0_535
	s_waitcnt lgkmcnt(0)
	buffer_inv sc1
	global_load_dword v2, v231, s[18:19] offset:1024 sc1
	s_add_u32 s36, s18, 0x2400
	s_addc_u32 s37, s19, 0
	s_waitcnt vmcnt(0)
	v_cmp_eq_u32_e32 vcc, v2, v1
	s_and_saveexec_b64 s[30:31], vcc
	s_cbranch_execz .LBB0_534
	s_add_u32 s34, s16, 0x4200
	s_addc_u32 s35, s17, 0
	s_mov_b32 s42, 1
	s_mov_b64 s[50:51], 0
	s_branch .LBB0_525

; __device__ __forceinline__ unsigned xb_ld(unsigned* p)              { return __hip_atomic_load(p, __ATOMIC_RELAXED, __HIP_MEMORY_SCOPE_AGENT); }
; #define XB_SPIN(cond, bar) do { unsigned _sp = 0; while (cond) { __builtin_amdgcn_s_sleep(1); \
;     if ((++_sp & 255u) == 0u) { if (xb_ld(&(bar)[XB_TMO])) break; if (_sp > XB_SPIN_CAP) { atomicAdd(&(bar)[XB_TMO], 1u); break; } } } } while (0)
; __device__ __forceinline__ void xcd_barrier(const XcdBarrier& b) {
;     ...
;         } else {
;             XB_SPIN(xb_ld(&bar[XB_XGEN(b.x)]) == gen, bar);
;             __builtin_amdgcn_fence(__ATOMIC_ACQUIRE, "agent");
;             asm volatile("s_waitcnt vmcnt(0)" ::: "memory");
;         }
.LBB0_534:
	s_or_b64 exec, exec, s[30:31]
	s_waitcnt vmcnt(0)
	s_waitcnt vmcnt(0)

; __device__ __forceinline__ unsigned xb_ld(unsigned* p)              { return __hip_atomic_load(p, __ATOMIC_RELAXED, __HIP_MEMORY_SCOPE_AGENT); }
; __device__ __forceinline__ unsigned xb_add(unsigned* p, unsigned v) { return __hip_atomic_fetch_add(p, v, __ATOMIC_RELAXED, __HIP_MEMORY_SCOPE_AGENT); }
; #define XB_SPIN(cond, bar) do { unsigned _sp = 0; while (cond) { __builtin_amdgcn_s_sleep(1); \
;     if ((++_sp & 255u) == 0u) { if (xb_ld(&(bar)[XB_TMO])) break; if (_sp > XB_SPIN_CAP) { atomicAdd(&(bar)[XB_TMO], 1u); break; } } } } while (0)
; __device__ __forceinline__ void xcd_barrier(const XcdBarrier& b) {
;     ...
;         const unsigned old = xb_add(&bar[XB_XSUB(b.x)], 1u);
;         const unsigned gen = old / nloc;
;         if (old + 1u == (gen + 1u) * nloc) {
;             __builtin_amdgcn_fence(__ATOMIC_RELEASE, "agent");
;             asm volatile("s_waitcnt vmcnt(0)" ::: "memory");
;             const unsigned og = xb_add(&bar[XB_TOP], 1u);
;             const unsigned tg = og / nx;
;             if (og + 1u == (tg + 1u) * nx) xb_add(&bar[XB_TOPGEN], 1u);
;             else XB_SPIN(xb_ld(&bar[XB_TOPGEN]) == tg, bar);
;             __builtin_amdgcn_fence(__ATOMIC_ACQUIRE, "agent");
;             xb_add(&bar[XB_XGEN(b.x)], 1u);
;             asm volatile("s_waitcnt vmcnt(0)" ::: "memory");
;         } else {
;             XB_SPIN(xb_ld(&bar[XB_XGEN(b.x)]) == gen, bar);
;             __builtin_amdgcn_fence(__ATOMIC_ACQUIRE, "agent");
;             asm volatile("s_waitcnt vmcnt(0)" ::: "memory");
;         }
.LBB0_699:
	s_or_b64 exec, exec, s[16:17]
	v_cvt_f32_u32_e32 v6, v4
	s_waitcnt vmcnt(0)
	v_readfirstlane_b32 s10, v5
	v_sub_u32_e32 v5, 0, v4
	v_rcp_iflag_f32_e32 v6, v6
	v_add_u32_e32 v7, s10, v1
	v_mul_f32_e32 v6, 0x4f7ffffe, v6
	v_cvt_u32_f32_e32 v6, v6
	v_mul_lo_u32 v1, v5, v6
	v_mul_hi_u32 v1, v6, v1
	v_add_u32_e32 v1, v6, v1
	v_mul_hi_u32 v1, v7, v1
	v_mul_lo_u32 v5, v1, v4
	v_sub_u32_e32 v5, v7, v5
	v_add_u32_e32 v6, 1, v1
	v_cmp_ge_u32_e32 vcc, v5, v4
	s_nop 1
	v_cndmask_b32_e32 v1, v1, v6, vcc
	v_sub_u32_e32 v6, v5, v4
	v_cndmask_b32_e32 v5, v5, v6, vcc
	v_add_u32_e32 v6, 1, v1
	v_cmp_ge_u32_e32 vcc, v5, v4
	v_add_u32_e32 v5, 1, v7
	s_nop 0
	v_cndmask_b32_e32 v1, v1, v6, vcc
	v_mul_lo_u32 v6, v4, v1
	v_add_u32_e32 v4, v6, v4
	v_cmp_ne_u32_e32 vcc, v5, v4
	s_and_saveexec_b64 s[10:11], vcc
	s_xor_b64 s[10:11], exec, s[10:11]
	s_mov_b32 s48, s58
	s_mov_b32 s49, s59
	s_cbranch_execz .LBB0_713
	s_waitcnt lgkmcnt(0)
	buffer_inv sc1
	global_load_dword v2, v231, s[4:5] offset:1024 sc1
	s_add_u32 s20, s4, 0x2400
	s_addc_u32 s21, s5, 0
	s_waitcnt vmcnt(0)
	v_cmp_eq_u32_e32 vcc, v2, v1
	s_and_saveexec_b64 s[16:17], vcc
	s_cbranch_execz .LBB0_712
	s_add_u32 s18, s2, 0x4200
	s_addc_u32 s19, s3, 0
	s_mov_b32 s36, 1
	s_mov_b64 s[30:31], 0
	s_branch .LBB0_703

; __device__ __forceinline__ unsigned xb_ld(unsigned* p)              { return __hip_atomic_load(p, __ATOMIC_RELAXED, __HIP_MEMORY_SCOPE_AGENT); }
; #define XB_SPIN(cond, bar) do { unsigned _sp = 0; while (cond) { __builtin_amdgcn_s_sleep(1); \
;     if ((++_sp & 255u) == 0u) { if (xb_ld(&(bar)[XB_TMO])) break; if (_sp > XB_SPIN_CAP) { atomicAdd(&(bar)[XB_TMO], 1u); break; } } } } while (0)
; __device__ __forceinline__ void xcd_barrier(const XcdBarrier& b) {
;     ...
;         } else {
;             XB_SPIN(xb_ld(&bar[XB_XGEN(b.x)]) == gen, bar);
;             __builtin_amdgcn_fence(__ATOMIC_ACQUIRE, "agent");
;             asm volatile("s_waitcnt vmcnt(0)" ::: "memory");
;         }
.LBB0_712:
	s_or_b64 exec, exec, s[16:17]
	s_waitcnt vmcnt(0)
	s_waitcnt vmcnt(0)

; __device__ __forceinline__ unsigned xb_ld(unsigned* p)              { return __hip_atomic_load(p, __ATOMIC_RELAXED, __HIP_MEMORY_SCOPE_AGENT); }
; __device__ __forceinline__ unsigned xb_add(unsigned* p, unsigned v) { return __hip_atomic_fetch_add(p, v, __ATOMIC_RELAXED, __HIP_MEMORY_SCOPE_AGENT); }
; #define XB_SPIN(cond, bar) do { unsigned _sp = 0; while (cond) { __builtin_amdgcn_s_sleep(1); \
;     if ((++_sp & 255u) == 0u) { if (xb_ld(&(bar)[XB_TMO])) break; if (_sp > XB_SPIN_CAP) { atomicAdd(&(bar)[XB_TMO], 1u); break; } } } } while (0)
; __device__ __forceinline__ void xcd_barrier(const XcdBarrier& b) {
;     ...
;         const unsigned old = xb_add(&bar[XB_XSUB(b.x)], 1u);
;         const unsigned gen = old / nloc;
;         if (old + 1u == (gen + 1u) * nloc) {
;             __builtin_amdgcn_fence(__ATOMIC_RELEASE, "agent");
;             asm volatile("s_waitcnt vmcnt(0)" ::: "memory");
;             const unsigned og = xb_add(&bar[XB_TOP], 1u);
;             const unsigned tg = og / nx;
;             if (og + 1u == (tg + 1u) * nx) xb_add(&bar[XB_TOPGEN], 1u);
;             else XB_SPIN(xb_ld(&bar[XB_TOPGEN]) == tg, bar);
;             __builtin_amdgcn_fence(__ATOMIC_ACQUIRE, "agent");
;             xb_add(&bar[XB_XGEN(b.x)], 1u);
;             asm volatile("s_waitcnt vmcnt(0)" ::: "memory");
;         } else {
;             XB_SPIN(xb_ld(&bar[XB_XGEN(b.x)]) == gen, bar);
;             __builtin_amdgcn_fence(__ATOMIC_ACQUIRE, "agent");
;             asm volatile("s_waitcnt vmcnt(0)" ::: "memory");
;         }
.LBB0_751:
	s_or_b64 exec, exec, s[8:9]
	v_cvt_f32_u32_e32 v6, v4
	s_waitcnt vmcnt(0)
	v_readfirstlane_b32 s6, v5
	v_sub_u32_e32 v5, 0, v4
	v_rcp_iflag_f32_e32 v6, v6
	v_add_u32_e32 v7, s6, v1
	v_mul_f32_e32 v6, 0x4f7ffffe, v6
	v_cvt_u32_f32_e32 v6, v6
	v_mul_lo_u32 v1, v5, v6
	v_mul_hi_u32 v1, v6, v1
	v_add_u32_e32 v1, v6, v1
	v_mul_hi_u32 v1, v7, v1
	v_mul_lo_u32 v5, v1, v4
	v_sub_u32_e32 v5, v7, v5
	v_add_u32_e32 v6, 1, v1
	v_cmp_ge_u32_e32 vcc, v5, v4
	s_nop 1
	v_cndmask_b32_e32 v1, v1, v6, vcc
	v_sub_u32_e32 v6, v5, v4
	v_cndmask_b32_e32 v5, v5, v6, vcc
	v_add_u32_e32 v6, 1, v1
	v_cmp_ge_u32_e32 vcc, v5, v4
	v_add_u32_e32 v5, 1, v7
	s_nop 0
	v_cndmask_b32_e32 v1, v1, v6, vcc
	v_mul_lo_u32 v6, v4, v1
	v_add_u32_e32 v4, v6, v4
	v_cmp_ne_u32_e32 vcc, v5, v4
	s_and_saveexec_b64 s[6:7], vcc
	s_xor_b64 s[6:7], exec, s[6:7]
	s_cbranch_execz .LBB0_765
	s_waitcnt lgkmcnt(0)
	buffer_inv sc1
	global_load_dword v2, v231, s[4:5] offset:1024 sc1
	s_add_u32 s14, s4, 0x2400
	s_addc_u32 s15, s5, 0
	s_waitcnt vmcnt(0)
	v_cmp_eq_u32_e32 vcc, v2, v1
	s_and_saveexec_b64 s[8:9], vcc
	s_cbranch_execz .LBB0_764
	s_add_u32 s10, s2, 0x4200
	s_addc_u32 s11, s3, 0
	s_mov_b32 s26, 1
	s_mov_b64 s[16:17], 0
	s_branch .LBB0_755

; __device__ __forceinline__ unsigned xb_ld(unsigned* p)              { return __hip_atomic_load(p, __ATOMIC_RELAXED, __HIP_MEMORY_SCOPE_AGENT); }
; __device__ __forceinline__ unsigned xb_add(unsigned* p, unsigned v) { return __hip_atomic_fetch_add(p, v, __ATOMIC_RELAXED, __HIP_MEMORY_SCOPE_AGENT); }
; #define XB_SPIN(cond, bar) do { unsigned _sp = 0; while (cond) { __builtin_amdgcn_s_sleep(1); \
;     if ((++_sp & 255u) == 0u) { if (xb_ld(&(bar)[XB_TMO])) break; if (_sp > XB_SPIN_CAP) { atomicAdd(&(bar)[XB_TMO], 1u); break; } } } } while (0)
; __device__ __forceinline__ void xcd_barrier(const XcdBarrier& b) {
;     ...
;         const unsigned old = xb_add(&bar[XB_XSUB(b.x)], 1u);
;         const unsigned gen = old / nloc;
;         if (old + 1u == (gen + 1u) * nloc) {
;             __builtin_amdgcn_fence(__ATOMIC_RELEASE, "agent");
;             asm volatile("s_waitcnt vmcnt(0)" ::: "memory");
;             const unsigned og = xb_add(&bar[XB_TOP], 1u);
;             const unsigned tg = og / nx;
;             if (og + 1u == (tg + 1u) * nx) xb_add(&bar[XB_TOPGEN], 1u);
;             else XB_SPIN(xb_ld(&bar[XB_TOPGEN]) == tg, bar);
;             __builtin_amdgcn_fence(__ATOMIC_ACQUIRE, "agent");
;             xb_add(&bar[XB_XGEN(b.x)], 1u);
;             asm volatile("s_waitcnt vmcnt(0)" ::: "memory");
;         } else {
;             XB_SPIN(xb_ld(&bar[XB_XGEN(b.x)]) == gen, bar);
;             __builtin_amdgcn_fence(__ATOMIC_ACQUIRE, "agent");
;             asm volatile("s_waitcnt vmcnt(0)" ::: "memory");
;         }
.LBB0_932:
	s_or_b64 exec, exec, s[14:15]
	v_cvt_f32_u32_e32 v6, v4
	s_waitcnt vmcnt(0)
	v_readfirstlane_b32 s6, v5
	v_sub_u32_e32 v5, 0, v4
	v_rcp_iflag_f32_e32 v6, v6
	v_add_u32_e32 v7, s6, v1
	v_mul_f32_e32 v6, 0x4f7ffffe, v6
	v_cvt_u32_f32_e32 v6, v6
	v_mul_lo_u32 v1, v5, v6
	v_mul_hi_u32 v1, v6, v1
	v_add_u32_e32 v1, v6, v1
	v_mul_hi_u32 v1, v7, v1
	v_mul_lo_u32 v5, v1, v4
	v_sub_u32_e32 v5, v7, v5
	v_add_u32_e32 v6, 1, v1
	v_cmp_ge_u32_e32 vcc, v5, v4
	s_nop 1
	v_cndmask_b32_e32 v1, v1, v6, vcc
	v_sub_u32_e32 v6, v5, v4
	v_cndmask_b32_e32 v5, v5, v6, vcc
	v_add_u32_e32 v6, 1, v1
	v_cmp_ge_u32_e32 vcc, v5, v4
	v_add_u32_e32 v5, 1, v7
	s_nop 0
	v_cndmask_b32_e32 v1, v1, v6, vcc
	v_mul_lo_u32 v6, v4, v1
	v_add_u32_e32 v4, v6, v4
	v_cmp_ne_u32_e32 vcc, v5, v4
	s_and_saveexec_b64 s[6:7], vcc
	v_readlane_b32 s26, v254, 34
	s_xor_b64 s[6:7], exec, s[6:7]
	v_readlane_b32 s27, v254, 35
	s_cbranch_execz .LBB0_946
	s_waitcnt lgkmcnt(0)
	buffer_inv sc1
	global_load_dword v2, v231, s[4:5] offset:1024 sc1
	s_add_u32 s30, s4, 0x2400
	s_addc_u32 s31, s5, 0
	s_waitcnt vmcnt(0)
	v_cmp_eq_u32_e32 vcc, v2, v1
	s_and_saveexec_b64 s[14:15], vcc
	s_cbranch_execz .LBB0_945
	s_add_u32 s20, s2, 0x4200
	s_addc_u32 s21, s3, 0
	s_mov_b32 s26, 1
	s_mov_b64 s[34:35], 0
	s_branch .LBB0_936

; __device__ __forceinline__ unsigned xb_ld(unsigned* p)              { return __hip_atomic_load(p, __ATOMIC_RELAXED, __HIP_MEMORY_SCOPE_AGENT); }
; #define XB_SPIN(cond, bar) do { unsigned _sp = 0; while (cond) { __builtin_amdgcn_s_sleep(1); \
;     if ((++_sp & 255u) == 0u) { if (xb_ld(&(bar)[XB_TMO])) break; if (_sp > XB_SPIN_CAP) { atomicAdd(&(bar)[XB_TMO], 1u); break; } } } } while (0)
; __device__ __forceinline__ void xcd_barrier(const XcdBarrier& b) {
;     ...
;         } else {
;             XB_SPIN(xb_ld(&bar[XB_XGEN(b.x)]) == gen, bar);
;             __builtin_amdgcn_fence(__ATOMIC_ACQUIRE, "agent");
;             asm volatile("s_waitcnt vmcnt(0)" ::: "memory");
;         }
.LBB0_945:
	s_or_b64 exec, exec, s[14:15]
	s_waitcnt vmcnt(0)
	s_waitcnt vmcnt(0)

; __device__ __forceinline__ unsigned xb_ld(unsigned* p)              { return __hip_atomic_load(p, __ATOMIC_RELAXED, __HIP_MEMORY_SCOPE_AGENT); }
; __device__ __forceinline__ unsigned xb_add(unsigned* p, unsigned v) { return __hip_atomic_fetch_add(p, v, __ATOMIC_RELAXED, __HIP_MEMORY_SCOPE_AGENT); }
; #define XB_SPIN(cond, bar) do { unsigned _sp = 0; while (cond) { __builtin_amdgcn_s_sleep(1); \
;     if ((++_sp & 255u) == 0u) { if (xb_ld(&(bar)[XB_TMO])) break; if (_sp > XB_SPIN_CAP) { atomicAdd(&(bar)[XB_TMO], 1u); break; } } } } while (0)
; __device__ __forceinline__ void xcd_barrier(const XcdBarrier& b) {
;     ...
;         const unsigned old = xb_add(&bar[XB_XSUB(b.x)], 1u);
;         const unsigned gen = old / nloc;
;         if (old + 1u == (gen + 1u) * nloc) {
;             __builtin_amdgcn_fence(__ATOMIC_RELEASE, "agent");
;             asm volatile("s_waitcnt vmcnt(0)" ::: "memory");
;             const unsigned og = xb_add(&bar[XB_TOP], 1u);
;             const unsigned tg = og / nx;
;             if (og + 1u == (tg + 1u) * nx) xb_add(&bar[XB_TOPGEN], 1u);
;             else XB_SPIN(xb_ld(&bar[XB_TOPGEN]) == tg, bar);
;             __builtin_amdgcn_fence(__ATOMIC_ACQUIRE, "agent");
;             xb_add(&bar[XB_XGEN(b.x)], 1u);
;             asm volatile("s_waitcnt vmcnt(0)" ::: "memory");
;         } else {
;             XB_SPIN(xb_ld(&bar[XB_XGEN(b.x)]) == gen, bar);
;             __builtin_amdgcn_fence(__ATOMIC_ACQUIRE, "agent");
;             asm volatile("s_waitcnt vmcnt(0)" ::: "memory");
;         }
.LBB0_1007:
	s_or_b64 exec, exec, s[16:17]
	v_cvt_f32_u32_e32 v6, v4
	s_waitcnt vmcnt(0)
	v_readfirstlane_b32 s2, v5
	v_sub_u32_e32 v5, 0, v4
	v_rcp_iflag_f32_e32 v6, v6
	v_add_u32_e32 v7, s2, v1
	v_mul_f32_e32 v6, 0x4f7ffffe, v6
	v_cvt_u32_f32_e32 v6, v6
	v_mul_lo_u32 v1, v5, v6
	v_mul_hi_u32 v1, v6, v1
	v_add_u32_e32 v1, v6, v1
	v_mul_hi_u32 v1, v7, v1
	v_mul_lo_u32 v5, v1, v4
	v_sub_u32_e32 v5, v7, v5
	v_add_u32_e32 v6, 1, v1
	v_cmp_ge_u32_e32 vcc, v5, v4
	s_nop 1
	v_cndmask_b32_e32 v1, v1, v6, vcc
	v_sub_u32_e32 v6, v5, v4
	v_cndmask_b32_e32 v5, v5, v6, vcc
	v_add_u32_e32 v6, 1, v1
	v_cmp_ge_u32_e32 vcc, v5, v4
	v_add_u32_e32 v5, 1, v7
	s_nop 0
	v_cndmask_b32_e32 v1, v1, v6, vcc
	v_mul_lo_u32 v6, v4, v1
	v_add_u32_e32 v4, v6, v4
	v_cmp_ne_u32_e32 vcc, v5, v4
	s_and_saveexec_b64 s[2:3], vcc
	v_readlane_b32 s26, v254, 34
	s_xor_b64 s[18:19], exec, s[2:3]
	v_readlane_b32 s27, v254, 35
	s_cbranch_execz .LBB0_1021
	s_waitcnt lgkmcnt(0)
	buffer_inv sc1
	global_load_dword v2, v231, s[6:7] offset:1024 sc1
	s_add_u32 s30, s6, 0x2400
	s_addc_u32 s31, s7, 0
	s_waitcnt vmcnt(0)
	v_cmp_eq_u32_e32 vcc, v2, v1
	s_and_saveexec_b64 s[2:3], vcc
	s_cbranch_execz .LBB0_1020
	s_add_u32 s20, s4, 0x4200
	s_addc_u32 s21, s5, 0
	s_mov_b32 s26, 1
	s_mov_b64 s[34:35], 0
	s_branch .LBB0_1011

; __device__ __forceinline__ unsigned xb_ld(unsigned* p)              { return __hip_atomic_load(p, __ATOMIC_RELAXED, __HIP_MEMORY_SCOPE_AGENT); }
; #define XB_SPIN(cond, bar) do { unsigned _sp = 0; while (cond) { __builtin_amdgcn_s_sleep(1); \
;     if ((++_sp & 255u) == 0u) { if (xb_ld(&(bar)[XB_TMO])) break; if (_sp > XB_SPIN_CAP) { atomicAdd(&(bar)[XB_TMO], 1u); break; } } } } while (0)
; __device__ __forceinline__ void xcd_barrier(const XcdBarrier& b) {
;     ...
;         } else {
;             XB_SPIN(xb_ld(&bar[XB_XGEN(b.x)]) == gen, bar);
;             __builtin_amdgcn_fence(__ATOMIC_ACQUIRE, "agent");
;             asm volatile("s_waitcnt vmcnt(0)" ::: "memory");
;         }
.LBB0_1020:
	s_or_b64 exec, exec, s[2:3]
	s_waitcnt vmcnt(0)
	s_waitcnt vmcnt(0)

; __device__ __forceinline__ unsigned xb_ld(unsigned* p)              { return __hip_atomic_load(p, __ATOMIC_RELAXED, __HIP_MEMORY_SCOPE_AGENT); }
; __device__ __forceinline__ unsigned xb_add(unsigned* p, unsigned v) { return __hip_atomic_fetch_add(p, v, __ATOMIC_RELAXED, __HIP_MEMORY_SCOPE_AGENT); }
; #define XB_SPIN(cond, bar) do { unsigned _sp = 0; while (cond) { __builtin_amdgcn_s_sleep(1); \
;     if ((++_sp & 255u) == 0u) { if (xb_ld(&(bar)[XB_TMO])) break; if (_sp > XB_SPIN_CAP) { atomicAdd(&(bar)[XB_TMO], 1u); break; } } } } while (0)
; __device__ __forceinline__ void xcd_barrier(const XcdBarrier& b) {
;     ...
;         const unsigned old = xb_add(&bar[XB_XSUB(b.x)], 1u);
;         const unsigned gen = old / nloc;
;         if (old + 1u == (gen + 1u) * nloc) {
;             __builtin_amdgcn_fence(__ATOMIC_RELEASE, "agent");
;             asm volatile("s_waitcnt vmcnt(0)" ::: "memory");
;             const unsigned og = xb_add(&bar[XB_TOP], 1u);
;             const unsigned tg = og / nx;
;             if (og + 1u == (tg + 1u) * nx) xb_add(&bar[XB_TOPGEN], 1u);
;             else XB_SPIN(xb_ld(&bar[XB_TOPGEN]) == tg, bar);
;             __builtin_amdgcn_fence(__ATOMIC_ACQUIRE, "agent");
;             xb_add(&bar[XB_XGEN(b.x)], 1u);
;             asm volatile("s_waitcnt vmcnt(0)" ::: "memory");
;         } else {
;             XB_SPIN(xb_ld(&bar[XB_XGEN(b.x)]) == gen, bar);
;             __builtin_amdgcn_fence(__ATOMIC_ACQUIRE, "agent");
;             asm volatile("s_waitcnt vmcnt(0)" ::: "memory");
;         }
.LBB0_1126:
	s_or_b64 exec, exec, s[8:9]
	v_cvt_f32_u32_e32 v6, v4
	s_waitcnt vmcnt(0)
	v_readfirstlane_b32 s2, v5
	v_sub_u32_e32 v5, 0, v4
	v_rcp_iflag_f32_e32 v6, v6
	v_add_u32_e32 v7, s2, v1
	v_mul_f32_e32 v6, 0x4f7ffffe, v6
	v_cvt_u32_f32_e32 v6, v6
	v_mul_lo_u32 v1, v5, v6
	v_mul_hi_u32 v1, v6, v1
	v_add_u32_e32 v1, v6, v1
	v_mul_hi_u32 v1, v7, v1
	v_mul_lo_u32 v5, v1, v4
	v_sub_u32_e32 v5, v7, v5
	v_add_u32_e32 v6, 1, v1
	v_cmp_ge_u32_e32 vcc, v5, v4
	s_nop 1
	v_cndmask_b32_e32 v1, v1, v6, vcc
	v_sub_u32_e32 v6, v5, v4
	v_cndmask_b32_e32 v5, v5, v6, vcc
	v_add_u32_e32 v6, 1, v1
	v_cmp_ge_u32_e32 vcc, v5, v4
	v_add_u32_e32 v5, 1, v7
	s_nop 0
	v_cndmask_b32_e32 v1, v1, v6, vcc
	v_mul_lo_u32 v6, v4, v1
	v_add_u32_e32 v4, v6, v4
	v_cmp_ne_u32_e32 vcc, v5, v4
	s_and_saveexec_b64 s[2:3], vcc
	v_readlane_b32 s26, v254, 34
	s_xor_b64 s[8:9], exec, s[2:3]
	v_readlane_b32 s27, v254, 35
	s_cbranch_execz .LBB0_1140
	s_waitcnt lgkmcnt(0)
	buffer_inv sc1
	global_load_dword v2, v231, s[6:7] offset:1024 sc1
	s_add_u32 s16, s6, 0x2400
	s_addc_u32 s17, s7, 0
	s_waitcnt vmcnt(0)
	v_cmp_eq_u32_e32 vcc, v2, v1
	s_and_saveexec_b64 s[2:3], vcc
	s_cbranch_execz .LBB0_1139
	s_add_u32 s10, s4, 0x4200
	s_addc_u32 s11, s5, 0
	s_mov_b32 s30, 1
	s_mov_b64 s[18:19], 0
	s_branch .LBB0_1130

; __device__ __forceinline__ unsigned xb_ld(unsigned* p)              { return __hip_atomic_load(p, __ATOMIC_RELAXED, __HIP_MEMORY_SCOPE_AGENT); }
; __device__ __forceinline__ unsigned xb_add(unsigned* p, unsigned v) { return __hip_atomic_fetch_add(p, v, __ATOMIC_RELAXED, __HIP_MEMORY_SCOPE_AGENT); }
; #define XB_SPIN(cond, bar) do { unsigned _sp = 0; while (cond) { __builtin_amdgcn_s_sleep(1); \
;     if ((++_sp & 255u) == 0u) { if (xb_ld(&(bar)[XB_TMO])) break; if (_sp > XB_SPIN_CAP) { atomicAdd(&(bar)[XB_TMO], 1u); break; } } } } while (0)
; __device__ __forceinline__ void xcd_barrier(const XcdBarrier& b) {
;     ...
;         const unsigned old = xb_add(&bar[XB_XSUB(b.x)], 1u);
;         const unsigned gen = old / nloc;
;         if (old + 1u == (gen + 1u) * nloc) {
;             __builtin_amdgcn_fence(__ATOMIC_RELEASE, "agent");
;             asm volatile("s_waitcnt vmcnt(0)" ::: "memory");
;             const unsigned og = xb_add(&bar[XB_TOP], 1u);
;             const unsigned tg = og / nx;
;             if (og + 1u == (tg + 1u) * nx) xb_add(&bar[XB_TOPGEN], 1u);
;             else XB_SPIN(xb_ld(&bar[XB_TOPGEN]) == tg, bar);
;             __builtin_amdgcn_fence(__ATOMIC_ACQUIRE, "agent");
;             xb_add(&bar[XB_XGEN(b.x)], 1u);
;             asm volatile("s_waitcnt vmcnt(0)" ::: "memory");
;         } else {
;             XB_SPIN(xb_ld(&bar[XB_XGEN(b.x)]) == gen, bar);
;             __builtin_amdgcn_fence(__ATOMIC_ACQUIRE, "agent");
;             asm volatile("s_waitcnt vmcnt(0)" ::: "memory");
;         }
.LBB0_1221:
	s_or_b64 exec, exec, s[14:15]
	v_cvt_f32_u32_e32 v6, v4
	s_waitcnt vmcnt(0)
	v_readfirstlane_b32 s2, v5
	v_sub_u32_e32 v5, 0, v4
	v_rcp_iflag_f32_e32 v6, v6
	v_add_u32_e32 v7, s2, v1
	v_mul_f32_e32 v6, 0x4f7ffffe, v6
	v_cvt_u32_f32_e32 v6, v6
	v_mul_lo_u32 v1, v5, v6
	v_mul_hi_u32 v1, v6, v1
	v_add_u32_e32 v1, v6, v1
	v_mul_hi_u32 v1, v7, v1
	v_mul_lo_u32 v5, v1, v4
	v_sub_u32_e32 v5, v7, v5
	v_add_u32_e32 v6, 1, v1
	v_cmp_ge_u32_e32 vcc, v5, v4
	s_nop 1
	v_cndmask_b32_e32 v1, v1, v6, vcc
	v_sub_u32_e32 v6, v5, v4
	v_cndmask_b32_e32 v5, v5, v6, vcc
	v_add_u32_e32 v6, 1, v1
	v_cmp_ge_u32_e32 vcc, v5, v4
	v_add_u32_e32 v5, 1, v7
	s_nop 0
	v_cndmask_b32_e32 v1, v1, v6, vcc
	v_mul_lo_u32 v6, v4, v1
	v_add_u32_e32 v4, v6, v4
	v_cmp_ne_u32_e32 vcc, v5, v4
	s_and_saveexec_b64 s[2:3], vcc
	v_readlane_b32 s26, v254, 34
	s_xor_b64 s[14:15], exec, s[2:3]
	v_readlane_b32 s27, v254, 35
	s_cbranch_execz .LBB0_1235
	s_waitcnt lgkmcnt(0)
	buffer_inv sc1
	global_load_dword v2, v231, s[10:11] offset:1024 sc1
	s_add_u32 s18, s10, 0x2400
	s_addc_u32 s19, s11, 0
	s_waitcnt vmcnt(0)
	v_cmp_eq_u32_e32 vcc, v2, v1
	s_and_saveexec_b64 s[2:3], vcc
	s_cbranch_execz .LBB0_1234
	s_add_u32 s16, s6, 0x4200
	s_addc_u32 s17, s7, 0
	s_mov_b32 s34, 1
	s_mov_b64 s[20:21], 0
	s_branch .LBB0_1225

; __device__ __forceinline__ unsigned xb_ld(unsigned* p)              { return __hip_atomic_load(p, __ATOMIC_RELAXED, __HIP_MEMORY_SCOPE_AGENT); }
; __device__ __forceinline__ unsigned xb_add(unsigned* p, unsigned v) { return __hip_atomic_fetch_add(p, v, __ATOMIC_RELAXED, __HIP_MEMORY_SCOPE_AGENT); }
; #define XB_SPIN(cond, bar) do { unsigned _sp = 0; while (cond) { __builtin_amdgcn_s_sleep(1); \
;     if ((++_sp & 255u) == 0u) { if (xb_ld(&(bar)[XB_TMO])) break; if (_sp > XB_SPIN_CAP) { atomicAdd(&(bar)[XB_TMO], 1u); break; } } } } while (0)
; __device__ __forceinline__ void xcd_barrier(const XcdBarrier& b) {
;     ...
;         const unsigned old = xb_add(&bar[XB_XSUB(b.x)], 1u);
;         const unsigned gen = old / nloc;
;         if (old + 1u == (gen + 1u) * nloc) {
;             __builtin_amdgcn_fence(__ATOMIC_RELEASE, "agent");
;             asm volatile("s_waitcnt vmcnt(0)" ::: "memory");
;             const unsigned og = xb_add(&bar[XB_TOP], 1u);
;             const unsigned tg = og / nx;
;             if (og + 1u == (tg + 1u) * nx) xb_add(&bar[XB_TOPGEN], 1u);
;             else XB_SPIN(xb_ld(&bar[XB_TOPGEN]) == tg, bar);
;             __builtin_amdgcn_fence(__ATOMIC_ACQUIRE, "agent");
;             xb_add(&bar[XB_XGEN(b.x)], 1u);
;             asm volatile("s_waitcnt vmcnt(0)" ::: "memory");
;         } else {
;             XB_SPIN(xb_ld(&bar[XB_XGEN(b.x)]) == gen, bar);
;             __builtin_amdgcn_fence(__ATOMIC_ACQUIRE, "agent");
;             asm volatile("s_waitcnt vmcnt(0)" ::: "memory");
;         }
.LBB0_1425:
	s_or_b64 exec, exec, s[10:11]
	v_cvt_f32_u32_e32 v6, v4
	s_waitcnt vmcnt(0)
	v_readfirstlane_b32 s2, v5
	v_sub_u32_e32 v5, 0, v4
	v_rcp_iflag_f32_e32 v6, v6
	v_add_u32_e32 v7, s2, v1
	v_mul_f32_e32 v6, 0x4f7ffffe, v6
	v_cvt_u32_f32_e32 v6, v6
	v_mul_lo_u32 v1, v5, v6
	v_mul_hi_u32 v1, v6, v1
	v_add_u32_e32 v1, v6, v1
	v_mul_hi_u32 v1, v7, v1
	v_mul_lo_u32 v5, v1, v4
	v_sub_u32_e32 v5, v7, v5
	v_add_u32_e32 v6, 1, v1
	v_cmp_ge_u32_e32 vcc, v5, v4
	s_nop 1
	v_cndmask_b32_e32 v1, v1, v6, vcc
	v_sub_u32_e32 v6, v5, v4
	v_cndmask_b32_e32 v5, v5, v6, vcc
	v_add_u32_e32 v6, 1, v1
	v_cmp_ge_u32_e32 vcc, v5, v4
	v_add_u32_e32 v5, 1, v7
	s_nop 0
	v_cndmask_b32_e32 v1, v1, v6, vcc
	v_mul_lo_u32 v6, v4, v1
	v_add_u32_e32 v4, v6, v4
	v_cmp_ne_u32_e32 vcc, v5, v4
	s_and_saveexec_b64 s[2:3], vcc
	v_readlane_b32 s26, v254, 34
	s_xor_b64 s[10:11], exec, s[2:3]
	v_readlane_b32 s27, v254, 35
	s_cbranch_execz .LBB0_1439
	s_waitcnt lgkmcnt(0)
	buffer_inv sc1
	global_load_dword v2, v231, s[6:7] offset:1024 sc1
	s_add_u32 s16, s6, 0x2400
	s_addc_u32 s17, s7, 0
	s_waitcnt vmcnt(0)
	v_cmp_eq_u32_e32 vcc, v2, v1
	s_and_saveexec_b64 s[2:3], vcc
	s_cbranch_execz .LBB0_1438
	s_add_u32 s14, s4, 0x4200
	s_addc_u32 s15, s5, 0
	s_mov_b32 s28, 1
	s_mov_b64 s[18:19], 0
	s_branch .LBB0_1429
